# pass A scoring with three result buffers: each head's MFMAs interleaved with the VALU of the head two back
# speedup vs baseline: 1.0484x; 1.0009x over previous
.LBB0_1308:
	s_waitcnt vmcnt(5)
	v_mfma_f32_16x16x32_bf16 v[130:133], v[116:119], v[0:3], 0
	v_mfma_f32_16x16x32_bf16 v[156:159], v[116:119], v[244:247], 0
	s_min_i32 s32, s15, s100
	s_cmp_lt_i32 s32, 85
	s_cselect_b32 vcc_lo, s101, 0
	s_mul_i32 s32, s32, 0x600
	s_add_i32 s32, s32, vcc_lo
	v_add_u32_e32 v231, s32, v230
	v_add_u32_e32 v222, s32, v197
	s_add_i32 s31, s15, 8
	s_min_i32 s35, s31, s14
	v_lshl_or_b32 v72, s35, 5, v125
	s_waitcnt vmcnt(3)
	v_mfma_f32_16x16x32_bf16 v[134:137], v[112:115], v[0:3], 0
	v_mfma_f32_16x16x32_bf16 v[160:163], v[112:115], v[244:247], 0
	v_ashrrev_i32_e32 v73, 31, v72
	v_lshlrev_b64 v[72:73], 7, v[72:73]
	v_sub_u32_e32 v72, v72, v229
	v_lshl_add_u64 v[84:85], v[120:121], 0, v[72:73]
	v_mfma_f32_16x16x32_bf16 v[138:141], v[108:111], v[4:7], v[130:133]
	v_mfma_f32_16x16x32_bf16 v[156:159], v[108:111], v[248:251], v[156:159]
	global_load_dwordx4 v[72:75], v[84:85], off
	global_load_dwordx4 v[76:79], v[84:85], off offset:1024
	global_load_dwordx4 v[80:83], v[84:85], off offset:2048
	s_nop 0
	global_load_dwordx4 v[84:87], v[84:85], off offset:3072
	global_store_dwordx4 v232, v[216:219], s[20:21]
	global_store_dwordx2 v223, v[220:221], s[20:21]
	s_nop 1
	s_nop 0
	s_add_i32 s15, s15, 16
	s_waitcnt vmcnt(8)
	v_mfma_f32_16x16x32_bf16 v[132:135], v[104:107], v[4:7], v[134:137]
	v_mfma_f32_16x16x32_bf16 v[160:163], v[104:107], v[248:251], v[160:163]
	s_min_i32 s35, s15, s14
	s_cmp_ge_i32 s31, s82
	v_mfma_f32_16x16x32_bf16 v[142:145], v[116:119], v[16:19], 0
	v_mfma_f32_16x16x32_bf16 v[146:149], v[112:115], v[16:19], 0
	v_mfma_f32_16x16x32_bf16 v[142:145], v[108:111], v[20:23], v[142:145]
	v_mfma_f32_16x16x32_bf16 v[146:149], v[104:107], v[20:23], v[146:149]
	s_nop 3
	v_mfma_f32_16x16x32_bf16 v[150:153], v[116:119], v[24:27], 0
	v_fma_f32 v156, v12, |v138|, v156
	v_fma_f32 v160, v12, |v132|, v160
	v_mfma_f32_16x16x32_bf16 v[224:227], v[112:115], v[24:27], 0
	v_fma_f32 v157, v12, |v139|, v157
	v_fma_f32 v161, v12, |v133|, v161
	v_mfma_f32_16x16x32_bf16 v[150:153], v[108:111], v[28:31], v[150:153]
	v_fma_f32 v158, v12, |v140|, v158
	v_fma_f32 v162, v12, |v134|, v162
	v_mfma_f32_16x16x32_bf16 v[224:227], v[104:107], v[28:31], v[224:227]
	v_fma_f32 v159, v12, |v141|, v159
	v_fma_f32 v163, v12, |v135|, v163
	v_mfma_f32_16x16x32_bf16 v[138:141], v[116:119], v[32:35], 0
	v_fma_f32 v156, v13, |v142|, v156
	v_fma_f32 v160, v13, |v146|, v160
	v_mfma_f32_16x16x32_bf16 v[132:135], v[112:115], v[32:35], 0
	v_fma_f32 v157, v13, |v143|, v157
	v_fma_f32 v161, v13, |v147|, v161
	v_mfma_f32_16x16x32_bf16 v[138:141], v[108:111], v[36:39], v[138:141]
	v_fma_f32 v158, v13, |v144|, v158
	v_fma_f32 v162, v13, |v148|, v162
	v_mfma_f32_16x16x32_bf16 v[132:135], v[104:107], v[36:39], v[132:135]
	v_fma_f32 v159, v13, |v145|, v159
	v_fma_f32 v163, v13, |v149|, v163
	v_mfma_f32_16x16x32_bf16 v[142:145], v[116:119], v[40:43], 0
	v_fma_f32 v156, v14, |v150|, v156
	v_fma_f32 v160, v14, |v224|, v160
	v_mfma_f32_16x16x32_bf16 v[146:149], v[112:115], v[40:43], 0
	v_fma_f32 v157, v14, |v151|, v157
	v_fma_f32 v161, v14, |v225|, v161
	v_mfma_f32_16x16x32_bf16 v[142:145], v[108:111], v[44:47], v[142:145]
	v_fma_f32 v158, v14, |v152|, v158
	v_fma_f32 v162, v14, |v226|, v162
	v_mfma_f32_16x16x32_bf16 v[146:149], v[104:107], v[44:47], v[146:149]
	v_fma_f32 v159, v14, |v153|, v159
	v_fma_f32 v163, v14, |v227|, v163
	v_mfma_f32_16x16x32_bf16 v[150:153], v[116:119], v[48:51], 0
	v_fma_f32 v156, v15, |v138|, v156
	v_fma_f32 v160, v15, |v132|, v160
	v_mfma_f32_16x16x32_bf16 v[224:227], v[112:115], v[48:51], 0
	v_fma_f32 v157, v15, |v139|, v157
	v_fma_f32 v161, v15, |v133|, v161
	v_mfma_f32_16x16x32_bf16 v[150:153], v[108:111], v[52:55], v[150:153]
	v_fma_f32 v158, v15, |v140|, v158
	v_fma_f32 v162, v15, |v134|, v162
	v_mfma_f32_16x16x32_bf16 v[224:227], v[104:107], v[52:55], v[224:227]
	v_fma_f32 v159, v15, |v141|, v159
	v_fma_f32 v163, v15, |v135|, v163
	v_mfma_f32_16x16x32_bf16 v[138:141], v[116:119], v[56:59], 0
	v_fma_f32 v156, v8, |v142|, v156
	v_fma_f32 v160, v8, |v146|, v160
	v_mfma_f32_16x16x32_bf16 v[132:135], v[112:115], v[56:59], 0
	v_fma_f32 v157, v8, |v143|, v157
	v_fma_f32 v161, v8, |v147|, v161
	v_mfma_f32_16x16x32_bf16 v[138:141], v[108:111], v[60:63], v[138:141]
	v_fma_f32 v158, v8, |v144|, v158
	v_fma_f32 v162, v8, |v148|, v162
	v_mfma_f32_16x16x32_bf16 v[132:135], v[104:107], v[60:63], v[132:135]
	v_fma_f32 v159, v8, |v145|, v159
	v_fma_f32 v163, v8, |v149|, v163
	v_mfma_f32_16x16x32_bf16 v[142:145], v[116:119], v[64:67], 0
	v_fma_f32 v156, v9, |v150|, v156
	v_fma_f32 v160, v9, |v224|, v160
	v_mfma_f32_16x16x32_bf16 v[146:149], v[112:115], v[64:67], 0
	v_fma_f32 v157, v9, |v151|, v157
	v_fma_f32 v161, v9, |v225|, v161
	v_mfma_f32_16x16x32_bf16 v[142:145], v[108:111], v[68:71], v[142:145]
	v_fma_f32 v158, v9, |v152|, v158
	v_fma_f32 v162, v9, |v226|, v162
	v_mfma_f32_16x16x32_bf16 v[146:149], v[104:107], v[68:71], v[146:149]
	v_fma_f32 v159, v9, |v153|, v159
	v_fma_f32 v163, v9, |v227|, v163
	v_fma_f32 v156, v10, |v138|, v156
	v_fma_f32 v160, v10, |v132|, v160
	v_fma_f32 v157, v10, |v139|, v157
	v_fma_f32 v161, v10, |v133|, v161
	v_fma_f32 v158, v10, |v140|, v158
	v_fma_f32 v162, v10, |v134|, v162
	v_fma_f32 v159, v10, |v141|, v159
	v_fma_f32 v163, v10, |v135|, v163
	v_fma_f32 v156, v11, |v142|, v156
	v_fma_f32 v160, v11, |v146|, v160
	v_fma_f32 v157, v11, |v143|, v157
	v_fma_f32 v161, v11, |v147|, v161
	v_fma_f32 v158, v11, |v144|, v158
	v_fma_f32 v162, v11, |v148|, v162
	v_fma_f32 v159, v11, |v145|, v159
	v_fma_f32 v163, v11, |v149|, v163
	s_nop 0
	v_lshrrev_b32 v104, 22, v156
	v_bfe_u32 v105, v156, 21, 1
	v_lshl_add_u32 v104, v104, 2, v128
	v_mad_u32_u24 v105, v105, s1, 1
	ds_add_u32 v104, v105
	v_lshrrev_b32 v104, 22, v157
	v_bfe_u32 v105, v157, 21, 1
	v_lshl_add_u32 v104, v104, 2, v128
	v_mad_u32_u24 v105, v105, s1, 1
	ds_add_u32 v104, v105
	v_lshrrev_b32 v104, 22, v158
	v_bfe_u32 v105, v158, 21, 1
	v_lshl_add_u32 v104, v104, 2, v128
	v_mad_u32_u24 v105, v105, s1, 1
	ds_add_u32 v104, v105
	v_lshrrev_b32 v104, 22, v159
	v_bfe_u32 v105, v159, 21, 1
	v_lshl_add_u32 v104, v104, 2, v128
	v_mad_u32_u24 v105, v105, s1, 1
	ds_add_u32 v104, v105
	v_lshrrev_b32 v104, 22, v160
	v_bfe_u32 v105, v160, 21, 1
	v_lshl_add_u32 v104, v104, 2, v128
	v_mad_u32_u24 v105, v105, s1, 1
	ds_add_u32 v104, v105
	v_lshrrev_b32 v104, 22, v161
	v_bfe_u32 v105, v161, 21, 1
	v_lshl_add_u32 v104, v104, 2, v128
	v_mad_u32_u24 v105, v105, s1, 1
	ds_add_u32 v104, v105
	v_lshrrev_b32 v104, 22, v162
	v_bfe_u32 v105, v162, 21, 1
	v_lshl_add_u32 v104, v104, 2, v128
	v_mad_u32_u24 v105, v105, s1, 1
	ds_add_u32 v104, v105
	v_lshrrev_b32 v104, 22, v163
	v_bfe_u32 v105, v163, 21, 1
	v_lshl_add_u32 v104, v104, 2, v128
	v_mad_u32_u24 v105, v105, s1, 1
	ds_add_u32 v104, v105
	v_lshl_or_b32 v104, s35, 5, v125
	v_ashrrev_i32_e32 v105, 31, v104
	v_lshlrev_b64 v[104:105], 7, v[104:105]
	v_sub_u32_e32 v104, v104, v229
	v_lshl_add_u64 v[104:105], v[120:121], 0, v[104:105]
	global_load_dwordx4 v[116:119], v[104:105], off
	global_load_dwordx4 v[108:111], v[104:105], off offset:1024
	global_load_dwordx4 v[112:115], v[104:105], off offset:2048
	s_nop 0
	global_load_dwordx4 v[104:107], v[104:105], off offset:3072
	v_perm_b32 v208, v157, v156, v168
	v_perm_b32 v209, v158, v157, v169
	v_perm_b32 v210, v159, v158, v170
	v_perm_b32 v211, v161, v160, v168
	v_perm_b32 v212, v162, v161, v169
	v_perm_b32 v213, v163, v162, v170
	global_store_dwordx4 v231, v[208:211], s[20:21]
	global_store_dwordx2 v222, v[212:213], s[20:21]
	s_cbranch_scc1 .LBB0_1307
	s_waitcnt vmcnt(11)
	v_mfma_f32_16x16x32_bf16 v[130:133], v[72:75], v[0:3], 0
	v_mfma_f32_16x16x32_bf16 v[164:167], v[72:75], v[244:247], 0
	s_min_i32 s32, s31, s100
	s_cmp_lt_i32 s32, 85
	s_cselect_b32 vcc_lo, s101, 0
	s_mul_i32 s32, s32, 0x600
	s_add_i32 s32, s32, vcc_lo
	v_add_u32_e32 v232, s32, v230
	v_add_u32_e32 v223, s32, v197
	s_waitcnt vmcnt(9)
	v_mfma_f32_16x16x32_bf16 v[134:137], v[80:83], v[0:3], 0
	v_mfma_f32_16x16x32_bf16 v[186:189], v[80:83], v[244:247], 0
	v_mfma_f32_16x16x32_bf16 v[138:141], v[76:79], v[4:7], v[130:133]
	v_mfma_f32_16x16x32_bf16 v[164:167], v[76:79], v[248:251], v[164:167]
	s_waitcnt vmcnt(8)
	v_mfma_f32_16x16x32_bf16 v[132:135], v[84:87], v[4:7], v[134:137]
	v_mfma_f32_16x16x32_bf16 v[186:189], v[84:87], v[248:251], v[186:189]
	v_mfma_f32_16x16x32_bf16 v[142:145], v[72:75], v[16:19], 0
	v_mfma_f32_16x16x32_bf16 v[146:149], v[80:83], v[16:19], 0
	v_mfma_f32_16x16x32_bf16 v[142:145], v[76:79], v[20:23], v[142:145]
	v_mfma_f32_16x16x32_bf16 v[146:149], v[84:87], v[20:23], v[146:149]
	s_nop 3
	v_mfma_f32_16x16x32_bf16 v[150:153], v[72:75], v[24:27], 0
	v_fma_f32 v164, v12, |v138|, v164
	v_fma_f32 v186, v12, |v132|, v186
	v_mfma_f32_16x16x32_bf16 v[224:227], v[80:83], v[24:27], 0
	v_fma_f32 v165, v12, |v139|, v165
	v_fma_f32 v187, v12, |v133|, v187
	v_mfma_f32_16x16x32_bf16 v[150:153], v[76:79], v[28:31], v[150:153]
	v_fma_f32 v166, v12, |v140|, v166
	v_fma_f32 v188, v12, |v134|, v188
	v_mfma_f32_16x16x32_bf16 v[224:227], v[84:87], v[28:31], v[224:227]
	v_fma_f32 v167, v12, |v141|, v167
	v_fma_f32 v189, v12, |v135|, v189
	v_mfma_f32_16x16x32_bf16 v[138:141], v[72:75], v[32:35], 0
	v_fma_f32 v164, v13, |v142|, v164
	v_fma_f32 v186, v13, |v146|, v186
	v_mfma_f32_16x16x32_bf16 v[132:135], v[80:83], v[32:35], 0
	v_fma_f32 v165, v13, |v143|, v165
	v_fma_f32 v187, v13, |v147|, v187
	v_mfma_f32_16x16x32_bf16 v[138:141], v[76:79], v[36:39], v[138:141]
	v_fma_f32 v166, v13, |v144|, v166
	v_fma_f32 v188, v13, |v148|, v188
	v_mfma_f32_16x16x32_bf16 v[132:135], v[84:87], v[36:39], v[132:135]
	v_fma_f32 v167, v13, |v145|, v167
	v_fma_f32 v189, v13, |v149|, v189
	v_mfma_f32_16x16x32_bf16 v[142:145], v[72:75], v[40:43], 0
	v_fma_f32 v164, v14, |v150|, v164
	v_fma_f32 v186, v14, |v224|, v186
	v_mfma_f32_16x16x32_bf16 v[146:149], v[80:83], v[40:43], 0
	v_fma_f32 v165, v14, |v151|, v165
	v_fma_f32 v187, v14, |v225|, v187
	v_mfma_f32_16x16x32_bf16 v[142:145], v[76:79], v[44:47], v[142:145]
	v_fma_f32 v166, v14, |v152|, v166
	v_fma_f32 v188, v14, |v226|, v188
	v_mfma_f32_16x16x32_bf16 v[146:149], v[84:87], v[44:47], v[146:149]
	v_fma_f32 v167, v14, |v153|, v167
	v_fma_f32 v189, v14, |v227|, v189
	v_mfma_f32_16x16x32_bf16 v[150:153], v[72:75], v[48:51], 0
	v_fma_f32 v164, v15, |v138|, v164
	v_fma_f32 v186, v15, |v132|, v186
	v_mfma_f32_16x16x32_bf16 v[224:227], v[80:83], v[48:51], 0
	v_fma_f32 v165, v15, |v139|, v165
	v_fma_f32 v187, v15, |v133|, v187
	v_mfma_f32_16x16x32_bf16 v[150:153], v[76:79], v[52:55], v[150:153]
	v_fma_f32 v166, v15, |v140|, v166
	v_fma_f32 v188, v15, |v134|, v188
	v_mfma_f32_16x16x32_bf16 v[224:227], v[84:87], v[52:55], v[224:227]
	v_fma_f32 v167, v15, |v141|, v167
	v_fma_f32 v189, v15, |v135|, v189
	v_mfma_f32_16x16x32_bf16 v[138:141], v[72:75], v[56:59], 0
	v_fma_f32 v164, v8, |v142|, v164
	v_fma_f32 v186, v8, |v146|, v186
	v_mfma_f32_16x16x32_bf16 v[132:135], v[80:83], v[56:59], 0
	v_fma_f32 v165, v8, |v143|, v165
	v_fma_f32 v187, v8, |v147|, v187
	v_mfma_f32_16x16x32_bf16 v[138:141], v[76:79], v[60:63], v[138:141]
	v_fma_f32 v166, v8, |v144|, v166
	v_fma_f32 v188, v8, |v148|, v188
	v_mfma_f32_16x16x32_bf16 v[132:135], v[84:87], v[60:63], v[132:135]
	v_fma_f32 v167, v8, |v145|, v167
	v_fma_f32 v189, v8, |v149|, v189
	v_mfma_f32_16x16x32_bf16 v[142:145], v[72:75], v[64:67], 0
	v_fma_f32 v164, v9, |v150|, v164
	v_fma_f32 v186, v9, |v224|, v186
	v_mfma_f32_16x16x32_bf16 v[146:149], v[80:83], v[64:67], 0
	v_fma_f32 v165, v9, |v151|, v165
	v_fma_f32 v187, v9, |v225|, v187
	v_mfma_f32_16x16x32_bf16 v[142:145], v[76:79], v[68:71], v[142:145]
	v_fma_f32 v166, v9, |v152|, v166
	v_fma_f32 v188, v9, |v226|, v188
	v_mfma_f32_16x16x32_bf16 v[146:149], v[84:87], v[68:71], v[146:149]
	v_fma_f32 v167, v9, |v153|, v167
	v_fma_f32 v189, v9, |v227|, v189
	v_fma_f32 v164, v10, |v138|, v164
	v_fma_f32 v186, v10, |v132|, v186
	v_fma_f32 v165, v10, |v139|, v165
	v_fma_f32 v187, v10, |v133|, v187
	v_fma_f32 v166, v10, |v140|, v166
	v_fma_f32 v188, v10, |v134|, v188
	v_fma_f32 v167, v10, |v141|, v167
	v_fma_f32 v189, v10, |v135|, v189
	v_fma_f32 v164, v11, |v142|, v164
	v_fma_f32 v186, v11, |v146|, v186
	v_fma_f32 v165, v11, |v143|, v165
	v_fma_f32 v187, v11, |v147|, v187
	v_fma_f32 v166, v11, |v144|, v166
	v_fma_f32 v188, v11, |v148|, v188
	v_fma_f32 v167, v11, |v145|, v167
	v_fma_f32 v189, v11, |v149|, v189
	v_lshrrev_b32 v135, 22, v164
	v_bfe_u32 v131, v164, 21, 1
	v_mad_u32_u24 v131, v131, s1, 1
	v_lshl_add_u32 v135, v135, 2, v128
	ds_add_u32 v135, v131
	v_lshrrev_b32 v131, 22, v165
	v_bfe_u32 v132, v165, 21, 1
	v_lshl_add_u32 v131, v131, 2, v128
	v_mad_u32_u24 v132, v132, s1, 1
	ds_add_u32 v131, v132
	v_lshrrev_b32 v131, 22, v166
	v_bfe_u32 v132, v166, 21, 1
	v_lshl_add_u32 v131, v131, 2, v128
	v_mad_u32_u24 v132, v132, s1, 1
	ds_add_u32 v131, v132
	v_lshrrev_b32 v131, 22, v167
	v_bfe_u32 v132, v167, 21, 1
	v_lshl_add_u32 v131, v131, 2, v128
	v_mad_u32_u24 v132, v132, s1, 1
	ds_add_u32 v131, v132
	v_lshrrev_b32 v131, 22, v186
	v_bfe_u32 v123, v186, 21, 1
	v_mad_u32_u24 v123, v123, s1, 1
	v_lshl_add_u32 v131, v131, 2, v128
	ds_add_u32 v131, v123
	v_lshrrev_b32 v123, 22, v187
	v_bfe_u32 v124, v187, 21, 1
	v_lshl_add_u32 v123, v123, 2, v128
	v_mad_u32_u24 v124, v124, s1, 1
	ds_add_u32 v123, v124
	v_lshrrev_b32 v123, 22, v188
	v_bfe_u32 v124, v188, 21, 1
	v_lshl_add_u32 v123, v123, 2, v128
	v_mad_u32_u24 v124, v124, s1, 1
	ds_add_u32 v123, v124
	v_lshrrev_b32 v123, 22, v189
	v_bfe_u32 v124, v189, 21, 1
	v_lshl_add_u32 v123, v123, 2, v128
	v_mad_u32_u24 v124, v124, s1, 1
	ds_add_u32 v123, v124
	v_perm_b32 v216, v165, v164, v168
	v_perm_b32 v217, v166, v165, v169
	v_perm_b32 v218, v167, v166, v170
	v_perm_b32 v219, v187, v186, v168
	v_perm_b32 v220, v188, v187, v169
	v_perm_b32 v221, v189, v188, v170
	s_cmp_ge_i32 s15, s82
	s_cbranch_scc0 .LBB0_1308
	global_store_dwordx4 v232, v[216:219], s[20:21]
	global_store_dwordx2 v223, v[220:221], s[20:21]
	s_branch .LBB0_1310
